# speedup vs baseline: 1.0231x; 1.0040x over previous
_Z10ode_kernelPKfPKDF16_S2_PfPKi:
	v_lshrrev_b32_e32 v167, 6, v0
	s_lshr_b32 s3, s2, 3
	v_add_u32_e32 v2, s3, v167
	s_load_dwordx4 s[4:7], s[0:1], 0x0
	s_load_dwordx2 s[12:13], s[0:1], 0x10
	v_and_b32_e32 v130, 3, v2
	v_and_b32_e32 v1, 63, v0
	v_readfirstlane_b32 s3, v130
	v_lshlrev_b32_e32 v166, 4, v1
	s_lshl_b32 s11, s3, 14
	v_lshl_or_b32 v2, v130, 17, v166
	v_mov_b32_e32 v3, 0
	s_and_b32 s17, s11, 0xc000
	s_mov_b32 s9, 0
	s_waitcnt lgkmcnt(0)
	v_lshl_add_u64 v[74:75], s[6:7], 0, v[2:3]
	s_lshl_b32 s8, s17, 1
	v_lshl_add_u64 v[46:47], v[74:75], 0, s[8:9]
	s_movk_i32 s15, 0x1000
	v_add_co_u32_e32 v18, vcc, s15, v46
	s_movk_i32 s14, 0x3000
	s_nop 0
	v_addc_co_u32_e32 v19, vcc, 0, v47, vcc
	v_add_co_u32_e32 v20, vcc, s14, v46
	s_lshl_b32 s10, s2, 10
	s_nop 0
	v_addc_co_u32_e32 v21, vcc, 0, v47, vcc
	s_and_b32 s8, s10, 0x3e000
	s_movk_i32 s16, 0x7000
	v_add_co_u32_e32 v48, vcc, s16, v46
	v_lshl_or_b32 v22, v1, 7, s8
	s_add_i32 s8, s11, 0x4000
	v_addc_co_u32_e32 v49, vcc, 0, v47, vcc
	s_movk_i32 s16, 0x5000
	s_and_b32 s8, s8, 0xc000
	v_add_co_u32_e32 v50, vcc, s16, v46
	s_lshl_b32 s8, s8, 1
	global_load_dwordx4 v[34:37], v[18:19], off offset:2048
	global_load_dwordx4 v[14:17], v[20:21], off offset:2048
	global_load_dwordx4 v[6:9], v[20:21], off offset:1024
	global_load_dwordx4 v[2:5], v[18:19], off offset:1024
	global_load_dwordx4 v[42:45], v[18:19], off offset:3072
	global_load_dwordx4 v[38:41], v[20:21], off offset:3072
	v_addc_co_u32_e32 v51, vcc, 0, v47, vcc
	v_lshl_add_u64 v[72:73], v[74:75], 0, s[8:9]
	v_add_co_u32_e32 v106, vcc, s14, v72
	global_load_dwordx4 v[10:13], v[50:51], off offset:1024
	global_load_dwordx4 v[52:55], v[50:51], off offset:2048
	global_load_dwordx4 v[56:59], v[48:49], off offset:2048
	v_addc_co_u32_e32 v107, vcc, 0, v73, vcc
	v_add_co_u32_e32 v108, vcc, s15, v72
	global_load_dwordx4 v[60:63], v[50:51], off offset:3072
	global_load_dwordx4 v[64:67], v[48:49], off offset:3072
	global_load_ushort v198, v22, s[12:13]
	v_addc_co_u32_e32 v109, vcc, 0, v73, vcc
	global_load_dwordx4 v[68:71], v[108:109], off offset:2048
	global_load_dwordx4 v[78:81], v[106:107], off offset:2048
	global_load_dwordx4 v[82:85], v[106:107], off offset:3072
	global_load_dwordx4 v[86:89], v[108:109], off offset:3072
	s_add_i32 s8, s11, 0x6000
	s_movk_i32 s16, 0x2000
	s_and_b32 s8, s8, 0xe000
	v_add_co_u32_e32 v26, vcc, s16, v46
	s_lshl_b32 s8, s8, 1
	s_nop 0
	v_addc_co_u32_e32 v27, vcc, 0, v47, vcc
	v_lshl_add_u64 v[110:111], v[74:75], 0, s[8:9]
	v_add_co_u32_e32 v112, vcc, s14, v110
	global_load_dwordx4 a[0:3], v[46:47], off
	global_load_dwordx4 a[8:11], v[46:47], off offset:1024
	global_load_dwordx4 a[12:15], v[26:27], off offset:1024
	global_load_dwordx4 a[20:23], v[26:27], off offset:2048
	global_load_dwordx4 a[16:19], v[46:47], off offset:2048
	global_load_dwordx4 a[24:27], v[46:47], off offset:3072
	global_load_dwordx4 a[4:7], v[20:21], off offset:-4096
	global_load_dwordx4 v[22:25], v[20:21], off
	global_load_dwordx4 a[28:31], v[26:27], off offset:3072
	s_nop 0
	global_load_dwordx4 v[18:21], v[18:19], off
	v_addc_co_u32_e32 v113, vcc, 0, v111, vcc
	v_add_co_u32_e32 v114, vcc, s15, v110
	v_lshl_or_b32 v199, v167, 15, v166
	s_nop 0
	v_addc_co_u32_e32 v115, vcc, 0, v111, vcc
	global_load_dwordx4 v[26:29], v[114:115], off offset:1024
	global_load_dwordx4 v[90:93], v[114:115], off offset:2048
	global_load_dwordx4 v[30:33], v[112:113], off offset:1024
	global_load_dwordx4 v[94:97], v[112:113], off offset:2048
	global_load_dwordx4 v[98:101], v[114:115], off offset:3072
	global_load_dwordx4 v[102:105], v[112:113], off offset:3072
	s_movk_i32 s8, 0x6000
	s_load_dwordx2 s[6:7], s[0:1], 0x20
	v_lshlrev_b32_e32 v76, 1, v0
	v_and_b32_e32 v200, 7, v0
	v_and_b32_e32 v128, 64, v76
	v_and_b32_e32 v179, 15, v0
	v_bfe_u32 v201, v0, 4, 1
	v_mov_b32_e32 v196, 0x44444444
	global_load_dwordx4 a[44:47], v[48:49], off offset:-4096
	s_waitcnt vmcnt(31)
	ds_write_b128 v199, v[14:17] offset:1024
	v_add_co_u32_e32 v14, vcc, s8, v46
	s_movk_i32 s8, 0x4000
	s_nop 0
	v_addc_co_u32_e32 v15, vcc, 0, v47, vcc
	s_waitcnt vmcnt(28)
	ds_write_b128 v199, v[42:45] offset:2048
	v_add_co_u32_e32 v42, vcc, s8, v46
	ds_write_b128 v199, v[34:37]
	s_nop 0
	v_addc_co_u32_e32 v43, vcc, 0, v47, vcc
	s_waitcnt vmcnt(27)
	ds_write_b128 v199, v[38:41] offset:3072
	v_add_co_u32_e32 v44, vcc, s16, v72
	global_load_dwordx4 a[36:39], v[14:15], off offset:1024
	global_load_dwordx4 a[32:35], v[42:43], off offset:1024
	global_load_dwordx4 a[48:51], v[42:43], off offset:2048
	global_load_dwordx4 a[52:55], v[14:15], off offset:2048
	global_load_dwordx4 a[60:63], v[14:15], off offset:3072
	global_load_dwordx4 a[40:43], v[50:51], off offset:-4096
	global_load_dwordx4 v[34:37], v[50:51], off
	global_load_dwordx4 v[38:41], v[48:49], off
	s_nop 0
	global_load_dwordx4 v[14:17], v[48:49], off offset:1024
	s_waitcnt vmcnt(34)
	ds_write_b128 v199, v[52:55] offset:4096
	s_waitcnt vmcnt(33)
	ds_write_b128 v199, v[56:59] offset:5120
	v_addc_co_u32_e32 v45, vcc, 0, v73, vcc
	s_xor_b32 s8, s17, 0x8000
	global_load_dwordx4 a[68:71], v[106:107], off offset:-4096
	s_waitcnt vmcnt(33)
	ds_write_b128 v199, v[60:63] offset:6144
	s_waitcnt vmcnt(32)
	ds_write_b128 v199, v[64:67] offset:7168
	v_add_co_u32_e32 v58, vcc, s16, v110
	s_lshl_b32 s8, s8, 1
	global_load_dwordx4 a[56:59], v[42:43], off offset:3072
	global_load_dwordx4 a[64:67], v[72:73], off
	global_load_dwordx4 a[72:75], v[72:73], off offset:1024
	global_load_dwordx4 a[80:83], v[72:73], off offset:2048
	global_load_dwordx4 a[84:87], v[44:45], off offset:2048
	global_load_dwordx4 a[92:95], v[44:45], off offset:3072
	global_load_dwordx4 a[76:79], v[44:45], off offset:1024
	global_load_dwordx4 a[88:91], v[72:73], off offset:3072
	global_load_dwordx4 v[46:49], v[106:107], off
	global_load_dwordx4 v[54:57], v[106:107], off offset:1024
	s_nop 0
	global_load_dwordx4 v[42:45], v[108:109], off
	global_load_dwordx4 v[50:53], v[108:109], off offset:1024
	s_waitcnt vmcnt(42)
	ds_write_b128 v199, v[68:71] offset:8192
	s_waitcnt vmcnt(41)
	ds_write_b128 v199, v[78:81] offset:9216
	s_waitcnt vmcnt(39)
	ds_write_b128 v199, v[86:89] offset:10240
	ds_write_b128 v199, v[82:85] offset:11264
	v_addc_co_u32_e32 v59, vcc, 0, v111, vcc
	v_lshl_add_u64 v[78:79], v[74:75], 0, s[8:9]
	v_add_co_u32_e32 v84, vcc, s14, v78
	global_load_dwordx4 a[96:99], v[110:111], off
	global_load_dwordx4 a[104:107], v[110:111], off offset:1024
	global_load_dwordx4 a[108:111], v[58:59], off offset:1024
	global_load_dwordx4 a[116:119], v[58:59], off offset:2048
	global_load_dwordx4 a[112:115], v[110:111], off offset:2048
	global_load_dwordx4 a[120:123], v[110:111], off offset:3072
	global_load_dwordx4 a[100:103], v[112:113], off offset:-4096
	global_load_dwordx4 v[62:65], v[112:113], off
	global_load_dwordx4 a[124:127], v[58:59], off offset:3072
	s_nop 0
	global_load_dwordx4 v[58:61], v[114:115], off
	v_addc_co_u32_e32 v85, vcc, 0, v79, vcc
	v_add_co_u32_e32 v82, vcc, s15, v78
	s_add_i32 s8, s11, 0xa000
	s_nop 0
	v_addc_co_u32_e32 v83, vcc, 0, v79, vcc
	global_load_dwordx4 v[110:113], v[82:83], off offset:2048
	global_load_dwordx4 v[106:109], v[84:85], off offset:2048
	s_waitcnt vmcnt(39)
	ds_write_b128 v199, v[90:93] offset:12288
	s_waitcnt vmcnt(37)
	ds_write_b128 v199, v[94:97] offset:13312
	s_waitcnt vmcnt(36)
	ds_write_b128 v199, v[98:101] offset:14336
	s_waitcnt vmcnt(35)
	ds_write_b128 v199, v[102:105] offset:15360
	global_load_dwordx4 a[128:131], v[78:79], off
	global_load_dwordx4 a[132:135], v[84:85], off offset:-4096
	global_load_dwordx4 a[136:139], v[78:79], off offset:1024
	global_load_dwordx4 a[144:147], v[78:79], off offset:2048
	global_load_dwordx4 v[102:105], v[82:83], off offset:3072
	global_load_dwordx4 v[98:101], v[84:85], off offset:3072
	s_and_b32 s8, s8, 0xe000
	v_add_co_u32_e32 v80, vcc, s16, v78
	s_lshl_b32 s8, s8, 1
	s_nop 0
	v_addc_co_u32_e32 v81, vcc, 0, v79, vcc
	v_lshl_add_u64 v[122:123], v[74:75], 0, s[8:9]
	v_add_co_u32_e32 v124, vcc, s14, v122
	s_add_i32 s8, s11, 0xc000
	s_nop 0
	v_addc_co_u32_e32 v125, vcc, 0, v123, vcc
	v_add_co_u32_e32 v126, vcc, s15, v122
	s_and_b32 s8, s8, 0xc000
	s_nop 0
	v_addc_co_u32_e32 v127, vcc, 0, v123, vcc
	global_load_dwordx4 v[70:73], v[124:125], off offset:1024
	global_load_dwordx4 v[114:117], v[124:125], off offset:2048
	global_load_dwordx4 v[66:69], v[126:127], off offset:1024
	global_load_dwordx4 v[118:121], v[126:127], off offset:2048
	global_load_dwordx4 a[148:151], v[80:81], off offset:2048
	global_load_dwordx4 a[156:159], v[80:81], off offset:3072
	global_load_dwordx4 v[132:135], v[126:127], off offset:3072
	global_load_dwordx4 v[136:139], v[124:125], off offset:3072
	global_load_dwordx4 a[140:143], v[80:81], off offset:1024
	global_load_dwordx4 a[152:155], v[78:79], off offset:3072
	s_nop 0
	global_load_dwordx4 v[78:81], v[84:85], off
	global_load_dwordx4 v[86:89], v[84:85], off offset:1024
	s_lshl_b32 s8, s8, 1
	v_lshl_add_u64 v[164:165], v[74:75], 0, s[8:9]
	v_add_co_u32_e32 v176, vcc, s14, v164
	s_add_i32 s11, s11, 0xe000
	s_nop 0
	v_addc_co_u32_e32 v177, vcc, 0, v165, vcc
	v_add_co_u32_e32 v184, vcc, s15, v164
	s_and_b32 s8, s11, 0xe000
	s_nop 0
	v_addc_co_u32_e32 v185, vcc, 0, v165, vcc
	global_load_dwordx4 v[140:143], v[184:185], off offset:2048
	global_load_dwordx4 v[144:147], v[176:177], off offset:2048
	global_load_dwordx4 v[148:151], v[176:177], off offset:3072
	global_load_dwordx4 v[152:155], v[184:185], off offset:3072
	s_lshl_b32 s8, s8, 1
	v_lshl_add_u64 v[186:187], v[74:75], 0, s[8:9]
	v_add_co_u32_e32 v188, vcc, s14, v186
	v_and_or_b32 v74, v76, 16, v200
	s_nop 0
	v_addc_co_u32_e32 v189, vcc, 0, v187, vcc
	v_add_co_u32_e32 v190, vcc, s15, v186
	v_lshlrev_b32_e32 v129, 2, v74
	s_nop 0
	v_addc_co_u32_e32 v191, vcc, 0, v187, vcc
	global_load_dwordx4 v[94:97], v[188:189], off offset:1024
	global_load_dwordx4 v[156:159], v[188:189], off offset:2048
	global_load_dwordx4 v[90:93], v[190:191], off offset:1024
	global_load_dwordx4 v[160:163], v[190:191], off offset:2048
	global_load_dwordx4 v[172:175], v[188:189], off offset:3072
	global_load_dwordx4 v[180:183], v[190:191], off offset:3072
	s_waitcnt lgkmcnt(0)
	global_load_dword v131, v129, s[6:7]
	global_load_dwordx4 v[74:77], v[82:83], off
	s_nop 0
	global_load_dwordx4 v[82:85], v[82:83], off offset:1024
	s_waitcnt vmcnt(32)
	ds_write_b128 v199, v[110:113] offset:16384
	s_waitcnt vmcnt(31)
	ds_write_b128 v199, v[106:109] offset:17408
	v_lshlrev_b32_e32 v106, 7, v130
	v_or3_b32 v202, v106, v128, v179
	v_lshlrev_b32_e32 v106, 9, v201
	v_or_b32_e32 v107, 32, v129
	v_or3_b32 v106, v106, s10, v202
	global_load_dword v178, v129, s[6:7] offset:128
	global_load_dword v192, v107, s[6:7] offset:128
	global_load_dword v193, v129, s[6:7] offset:32
	v_ashrrev_i32_e32 v107, 31, v106
	v_lshl_add_u64 v[128:129], v[106:107], 2, s[4:5]
	global_load_dword v171, v[128:129], off
	s_waitcnt vmcnt(30)
	ds_write_b128 v199, v[102:105] offset:18432
	s_waitcnt vmcnt(29)
	ds_write_b128 v199, v[98:101] offset:19456
	v_add_co_u32_e32 v98, vcc, s16, v122
	s_mov_b32 s14, 0x45000000
	s_nop 0
	v_addc_co_u32_e32 v99, vcc, 0, v123, vcc
	global_load_dwordx4 a[160:163], v[122:123], off
	global_load_dwordx4 a[168:171], v[122:123], off offset:1024
	global_load_dwordx4 a[172:175], v[98:99], off offset:1024
	global_load_dwordx4 a[180:183], v[98:99], off offset:2048
	global_load_dwordx4 a[176:179], v[122:123], off offset:2048
	global_load_dwordx4 a[184:187], v[122:123], off offset:3072
	global_load_dword v170, v[128:129], off offset:64
	global_load_dwordx4 a[164:167], v[124:125], off offset:-4096
	global_load_dwordx4 v[102:105], v[124:125], off
	global_load_dwordx4 a[188:191], v[98:99], off offset:3072
	s_nop 0
	global_load_dwordx4 v[98:101], v[126:127], off
	s_waitcnt vmcnt(36)
	ds_write_b128 v199, v[118:121] offset:20480
	ds_write_b128 v199, v[114:117] offset:21504
	global_load_dword v169, v[128:129], off offset:128
	v_add_co_u32_e32 v106, vcc, s16, v164
	s_waitcnt vmcnt(34)
	ds_write_b128 v199, v[132:135] offset:22528
	s_waitcnt vmcnt(33)
	ds_write_b128 v199, v[136:139] offset:23552
	v_addc_co_u32_e32 v107, vcc, 0, v165, vcc
	global_load_dwordx4 a[192:195], v[164:165], off
	global_load_dwordx4 a[196:199], v[176:177], off offset:-4096
	global_load_dwordx4 a[200:203], v[164:165], off offset:1024
	global_load_dwordx4 a[208:211], v[164:165], off offset:2048
	global_load_dwordx4 a[212:215], v[106:107], off offset:2048
	global_load_dwordx4 a[220:223], v[106:107], off offset:3072
	global_load_dwordx4 a[204:207], v[106:107], off offset:1024
	global_load_dwordx4 a[216:219], v[164:165], off offset:3072
	global_load_dwordx4 v[110:113], v[176:177], off
	global_load_dwordx4 v[118:121], v[176:177], off offset:1024
	s_nop 0
	global_load_dwordx4 v[106:109], v[184:185], off
	global_load_dwordx4 v[114:117], v[184:185], off offset:1024
	global_load_dword v168, v[128:129], off offset:192
	v_add_co_u32_e32 v122, vcc, s16, v186
	v_and_b32_e32 v133, 32, v0
	s_nop 0
	v_addc_co_u32_e32 v123, vcc, 0, v187, vcc
	s_waitcnt vmcnt(41)
	ds_write_b128 v199, v[140:143] offset:24576
	s_waitcnt vmcnt(40)
	ds_write_b128 v199, v[144:147] offset:25600
	s_waitcnt vmcnt(38)
	ds_write_b128 v199, v[152:155] offset:26624
	ds_write_b128 v199, v[148:151] offset:27648
	global_load_dwordx4 a[224:227], v[186:187], off
	global_load_dwordx4 a[232:235], v[186:187], off offset:1024
	global_load_dwordx4 a[236:239], v[122:123], off offset:1024
	global_load_dwordx4 a[244:247], v[122:123], off offset:2048
	global_load_dwordx4 a[240:243], v[186:187], off offset:2048
	global_load_dwordx4 a[248:251], v[186:187], off offset:3072
	global_load_dwordx4 a[228:231], v[188:189], off offset:-4096
	global_load_dwordx4 v[126:129], v[188:189], off
	global_load_dwordx4 a[252:255], v[122:123], off offset:3072
	s_nop 0
	global_load_dwordx4 v[122:125], v[190:191], off
	v_lshlrev_b32_e32 v132, 2, v201
	v_lshl_or_b32 v130, v130, 6, v133
	v_lshrrev_b32_e32 v139, 1, v0
	v_and_b32_e32 v203, 24, v139
	s_waitcnt vmcnt(44)
	ds_write_b128 v199, v[160:163] offset:28672
	ds_write_b128 v199, v[156:159] offset:29696
	s_waitcnt vmcnt(42)
	ds_write_b128 v199, v[180:183] offset:30720
	ds_write_b128 v199, v[172:175] offset:31744
	s_waitcnt vmcnt(10) lgkmcnt(0)
	v_lshrrev_b32_e32 v222, 2, v131
	v_and_or_b32 v222, v222, 8, v132
	v_mul_u32_u24_e32 v222, 0x110, v222
	v_and_or_b32 v223, v131, 31, v130
	v_add_lshl_u32 v223, v223, v222, 1
	v_or_b32_e32 v204, 0x20000, v223
	v_lshrrev_b32_e32 v222, 2, v178
	v_and_or_b32 v222, v222, 8, v132
	v_mul_u32_u24_e32 v222, 0x110, v222
	v_and_or_b32 v223, v178, 31, v130
	v_add_lshl_u32 v223, v223, v222, 1
	v_or_b32_e32 v205, 0x20000, v223
	v_lshrrev_b32_e32 v222, 2, v193
	v_and_or_b32 v222, v222, 8, v132
	v_mul_u32_u24_e32 v222, 0x110, v222
	v_and_or_b32 v223, v193, 31, v130
	v_add_lshl_u32 v223, v223, v222, 1
	v_or_b32_e32 v206, 0x20000, v223
	v_lshrrev_b32_e32 v222, 2, v192
	v_and_or_b32 v222, v222, 8, v132
	v_mul_u32_u24_e32 v222, 0x110, v222
	v_and_or_b32 v223, v192, 31, v130
	v_add_lshl_u32 v223, v223, v222, 1
	v_or_b32_e32 v207, 0x20000, v223
	s_movk_i32 s43, 0x110
	v_mad_u32_u24 v224, v179, s43, v203
	v_mov_b32_e32 v225, 0x20000
	v_lshl_or_b32 v224, v224, 1, v225
	s_lshl_b32 s43, s3, 1
	s_add_u32 s52, s43, 0
	s_and_b32 s52, s52, 7
	s_lshl_b32 s52, s52, 6
	s_nop 0
	v_add_u32_e32 v208, s52, v224
	s_add_u32 s52, s43, 1
	s_and_b32 s52, s52, 7
	s_lshl_b32 s52, s52, 6
	s_sub_u32 s52, s52, 64
	s_nop 0
	v_add_u32_e32 v209, s52, v224
	s_add_u32 s52, s43, 2
	s_and_b32 s52, s52, 7
	s_lshl_b32 s52, s52, 6
	s_nop 0
	v_add_u32_e32 v211, s52, v224
	s_add_u32 s52, s43, 3
	s_and_b32 s52, s52, 7
	s_lshl_b32 s52, s52, 6
	s_nop 0
	v_add_u32_e32 v212, s52, v224
	s_add_u32 s52, s43, 4
	s_and_b32 s52, s52, 7
	s_lshl_b32 s52, s52, 6
	s_nop 0
	v_add_u32_e32 v213, s52, v224
	s_add_u32 s52, s43, 5
	s_and_b32 s52, s52, 7
	s_lshl_b32 s52, s52, 6
	s_nop 0
	v_add_u32_e32 v214, s52, v224
	s_add_u32 s52, s43, 6
	s_and_b32 s52, s52, 7
	s_lshl_b32 s52, s52, 6
	s_nop 0
	v_add_u32_e32 v215, s52, v224
	s_add_u32 s52, s43, 7
	s_and_b32 s52, s52, 7
	s_lshl_b32 s52, s52, 6
	s_nop 0
	v_add_u32_e32 v216, s52, v224
	v_and_b32_e32 v225, 8, v0
	v_cmp_eq_u32_e32 vcc, 0, v225
	v_mov_b32_e32 v225, 0xeeeeeeee
	s_nop 1
	v_cndmask_b32_e32 v210, v225, v196, vcc
	v_and_b32_e32 v225, 47, v0
	v_cmp_eq_u32_e64 s[4:5], 0, v225
	v_lshlrev_b32_e32 v225, 4, v167
	v_lshlrev_b32_e32 v226, 3, v201
	s_mov_b32 s52, 0x24400
	v_or3_b32 v218, v225, v226, s52
	s_load_dwordx2 s[6:7], s[0:1], 0x18
	s_lshl_b32 s11, s2, 9
	s_mov_b64 s[22:23], 0
	s_mov_b32 s29, 0
	s_mov_b32 s30, 0
	v_mov_b32_e32 v221, 0
	s_mov_b32 s40, 0x3a000000
	s_mov_b32 s41, 0x34800000
	s_mov_b32 s42, 0x45000000
	v_mov_b32_e32 v217, 0x24480
	v_mov_b64_e32 v[230:231], 0
	v_mov_b64_e32 v[232:233], 0
	v_mov_b64_e32 v[234:235], 0
	v_mov_b64_e32 v[236:237], 0
	v_mov_b64_e32 v[238:239], 0
	v_mov_b64_e32 v[240:241], 0
	v_mov_b64_e32 v[242:243], 0
	v_mov_b64_e32 v[244:245], 0
	ds_write_b128 v217, v[230:233]
	v_mov_b32_e32 v178, 0
	v_fma_mixlo_f16 v131, v178, v238, v171
	v_fma_mixlo_f16 v139, v178, v238, v170
	v_fma_mixlo_f16 v147, v178, v238, v169
	v_fma_mixlo_f16 v155, v178, v238, v168
	v_fma_f32 v130, v178, v238, v171
	v_fma_f32 v138, v178, v238, v170
	v_fma_f32 v146, v178, v238, v169
	v_fma_f32 v154, v178, v238, v168
	v_fma_mix_f32 v130, v130, 1.0, -v131 op_sel_hi:[0,0,1]
	v_fma_mix_f32 v138, v138, 1.0, -v139 op_sel_hi:[0,0,1]
	v_fma_mix_f32 v146, v146, 1.0, -v147 op_sel_hi:[0,0,1]
	v_fma_mix_f32 v154, v154, 1.0, -v155 op_sel_hi:[0,0,1]
	v_fma_mixlo_f16 v133, v130, s42, 0
	v_fma_mixlo_f16 v141, v138, s42, 0
	v_fma_mixlo_f16 v149, v146, s42, 0
	v_fma_mixlo_f16 v157, v154, s42, 0
	v_fma_mix_f32 v130, v130, s42, -v133 op_sel_hi:[0,0,1]
	v_fma_mix_f32 v138, v138, s42, -v141 op_sel_hi:[0,0,1]
	v_fma_mix_f32 v146, v146, s42, -v149 op_sel_hi:[0,0,1]
	v_fma_mix_f32 v154, v154, s42, -v157 op_sel_hi:[0,0,1]
	v_fma_mixlo_f16 v132, v130, s42, 0
	v_fma_mixlo_f16 v140, v138, s42, 0
	v_fma_mixlo_f16 v148, v146, s42, 0
	v_fma_mixlo_f16 v156, v154, s42, 0
	ds_write_b16 v204, v131
	ds_write_b16 v205, v139
	ds_write_b16 v206, v147
	ds_write_b16 v207, v155
	ds_write_b16 v204, v133 offset:544
	ds_write_b16 v205, v141 offset:544
	ds_write_b16 v206, v149 offset:544
	ds_write_b16 v207, v157 offset:544
	ds_write_b16 v204, v132 offset:1088
	ds_write_b16 v205, v140 offset:1088
	ds_write_b16 v206, v148 offset:1088
	ds_write_b16 v207, v156 offset:1088
	ds_read_b128 v[180:183], v199 offset:0
	s_waitcnt lgkmcnt(6)
	ds_read_b128 v[184:187], v199 offset:1024
	ds_read_b128 v[188:191], v199 offset:4096
	ds_read_b128 v[192:195], v199 offset:5120
	ds_read_b128 v[222:225], v199 offset:8192
	ds_read_b128 v[226:229], v199 offset:9216
	s_mov_b32 s52, 0x3a83126f
	v_mov_b32_e32 v248, 0x358637bd
	s_waitcnt lgkmcnt(0)
	s_barrier
	ds_read_b128 v[130:133], v208
	ds_read_b128 v[134:137], v209 offset:64
	ds_read_b128 v[138:141], v211
	ds_read_b128 v[142:145], v212
	ds_read_b128 v[146:149], v213
	ds_read_b128 v[150:153], v214
	ds_read_b128 v[154:157], v215
	ds_read_b128 v[158:161], v216
	s_waitcnt lgkmcnt(7)
	v_smfmac_f32_16x16x64_f16 v[230:233], v[130:133], a[16:23], v210
	v_fma_f32 v179, |v171|, s52, v248
	v_fma_f32 v196, |v170|, s52, v248
	v_smfmac_f32_16x16x64_f16 v[234:237], v[130:133], v[180:187], v210
	ds_read_b128 v[180:183], v199 offset:12288
	ds_read_b128 v[184:187], v199 offset:13312
	v_fma_f32 v197, |v169|, s52, v248
	s_waitcnt lgkmcnt(8)
	v_smfmac_f32_16x16x64_f16 v[230:233], v[134:137], a[48:55], v210
	v_fma_f32 v198, |v168|, s52, v248
	v_smfmac_f32_16x16x64_f16 v[234:237], v[134:137], v[188:195], v210
	ds_read_b128 v[188:191], v199 offset:16384
	ds_read_b128 v[192:195], v199 offset:17408
	v_rcp_f32_e32 v179, v179
	s_waitcnt lgkmcnt(9)
	v_smfmac_f32_16x16x64_f16 v[230:233], v[138:141], a[80:87], v210
	v_rcp_f32_e32 v196, v196
	v_smfmac_f32_16x16x64_f16 v[234:237], v[138:141], v[222:229], v210
	ds_read_b128 v[222:225], v199 offset:20480
	ds_read_b128 v[226:229], v199 offset:21504
	v_rcp_f32_e32 v197, v197
	s_waitcnt lgkmcnt(10)
	v_smfmac_f32_16x16x64_f16 v[230:233], v[142:145], a[112:119], v210
	v_rcp_f32_e32 v198, v198
	s_waitcnt lgkmcnt(4)
	v_smfmac_f32_16x16x64_f16 v[234:237], v[142:145], v[180:187], v210
	ds_read_b128 v[180:183], v199 offset:24576
	ds_read_b128 v[184:187], v199 offset:25600
	v_mul_f32_e32 v249, v170, v196
	v_smfmac_f32_16x16x64_f16 v[230:233], v[146:149], a[144:151], v210
	v_mul_f32_e32 v166, v249, v249
	s_waitcnt lgkmcnt(4)
	v_smfmac_f32_16x16x64_f16 v[234:237], v[146:149], v[188:195], v210
	ds_read_b128 v[188:191], v199 offset:28672
	ds_read_b128 v[192:195], v199 offset:29696
	v_mul_f32_e32 v249, v171, v179
	v_smfmac_f32_16x16x64_f16 v[230:233], v[150:153], a[176:183], v210
	v_fmac_f32_e32 v166, v249, v249
	s_waitcnt lgkmcnt(4)
	v_smfmac_f32_16x16x64_f16 v[234:237], v[150:153], v[222:229], v210
	ds_read_b128 v[222:225], v199 offset:2048
	ds_read_b128 v[226:229], v199 offset:3072
	v_mul_f32_e32 v249, v169, v197
	v_smfmac_f32_16x16x64_f16 v[230:233], v[154:157], a[208:215], v210
	v_fmac_f32_e32 v166, v249, v249
	s_waitcnt lgkmcnt(4)
	v_smfmac_f32_16x16x64_f16 v[234:237], v[154:157], v[180:187], v210
	ds_read_b128 v[180:183], v199 offset:6144
	ds_read_b128 v[184:187], v199 offset:7168
	v_mul_f32_e32 v249, v168, v198
	s_waitcnt vmcnt(0)
	v_smfmac_f32_16x16x64_f16 v[230:233], v[158:161], a[240:247], v210
	v_fmac_f32_e32 v166, v249, v249
	s_waitcnt lgkmcnt(4)
	v_smfmac_f32_16x16x64_f16 v[234:237], v[158:161], v[188:195], v210
	ds_read_b128 v[188:191], v199 offset:10240
	ds_read_b128 v[192:195], v199 offset:11264
	v_smfmac_f32_16x16x64_f16 v[238:241], v[130:133], a[24:31], v210
	s_waitcnt lgkmcnt(4)
	v_smfmac_f32_16x16x64_f16 v[242:245], v[130:133], v[222:229], v210
	ds_read_b128 v[222:225], v199 offset:14336
	ds_read_b128 v[226:229], v199 offset:15360
	v_smfmac_f32_16x16x64_f16 v[238:241], v[134:137], a[56:63], v210
	v_fmac_f32_e32 v230, s40, v231
	s_waitcnt lgkmcnt(4)
	v_smfmac_f32_16x16x64_f16 v[242:245], v[134:137], v[180:187], v210
	ds_read_b128 v[180:183], v199 offset:18432
	ds_read_b128 v[184:187], v199 offset:19456
	v_fmac_f32_e32 v234, s40, v235
	v_smfmac_f32_16x16x64_f16 v[238:241], v[138:141], a[88:95], v210
	v_fmac_f32_e32 v230, s41, v232
	s_waitcnt lgkmcnt(4)
	v_smfmac_f32_16x16x64_f16 v[242:245], v[138:141], v[188:195], v210
	ds_read_b128 v[188:191], v199 offset:22528
	ds_read_b128 v[192:195], v199 offset:23552
	v_fmac_f32_e32 v234, s41, v236
	v_smfmac_f32_16x16x64_f16 v[238:241], v[142:145], a[120:127], v210
	s_nop 0
	v_permlane32_swap_b32_e32 v230, v234
	s_waitcnt lgkmcnt(4)
	v_smfmac_f32_16x16x64_f16 v[242:245], v[142:145], v[222:229], v210
	ds_read_b128 v[222:225], v199 offset:26624
	ds_read_b128 v[226:229], v199 offset:27648
	v_add_f32_e32 v175, v230, v234
	v_smfmac_f32_16x16x64_f16 v[238:241], v[146:149], a[152:159], v210
	ds_read_b128 v[230:233], v217
	s_waitcnt lgkmcnt(5)
	v_smfmac_f32_16x16x64_f16 v[242:245], v[146:149], v[180:187], v210
	ds_read_b128 v[180:183], v199 offset:30720
	ds_read_b128 v[184:187], v199 offset:31744
	ds_read_b128 v[234:237], v217
	v_smfmac_f32_16x16x64_f16 v[238:241], v[150:153], a[184:191], v210
	s_waitcnt lgkmcnt(6)
	v_smfmac_f32_16x16x64_f16 v[242:245], v[150:153], v[188:195], v210
	v_smfmac_f32_16x16x64_f16 v[238:241], v[154:157], a[216:223], v210
	s_waitcnt lgkmcnt(4)
	v_smfmac_f32_16x16x64_f16 v[242:245], v[154:157], v[222:229], v210
	v_smfmac_f32_16x16x64_f16 v[238:241], v[158:161], a[248:255], v210
	s_waitcnt lgkmcnt(1)
	v_smfmac_f32_16x16x64_f16 v[242:245], v[158:161], v[180:187], v210
	v_smfmac_f32_16x16x64_f16 v[230:233], v[130:133], a[0:7], v210
	s_waitcnt lgkmcnt(0)
	v_smfmac_f32_16x16x64_f16 v[234:237], v[130:133], v[18:25], v210
	v_smfmac_f32_16x16x64_f16 v[230:233], v[134:137], a[40:47], v210
	v_fmac_f32_e32 v238, s40, v239
	v_smfmac_f32_16x16x64_f16 v[234:237], v[134:137], v[34:41], v210
	v_fmac_f32_e32 v242, s40, v243
	v_smfmac_f32_16x16x64_f16 v[230:233], v[138:141], a[64:71], v210
	v_fmac_f32_e32 v238, s41, v240
	v_smfmac_f32_16x16x64_f16 v[234:237], v[138:141], v[42:49], v210
	v_fmac_f32_e32 v242, s41, v244
	v_smfmac_f32_16x16x64_f16 v[230:233], v[142:145], a[96:103], v210
	s_nop 0
	v_permlane32_swap_b32_e32 v238, v242
	v_smfmac_f32_16x16x64_f16 v[234:237], v[142:145], v[58:65], v210
	v_add_f32_e32 v174, v238, v242
	v_smfmac_f32_16x16x64_f16 v[230:233], v[146:149], a[128:135], v210
	ds_read_b128 v[238:241], v217
	v_smfmac_f32_16x16x64_f16 v[234:237], v[146:149], v[74:81], v210
	ds_read_b128 v[242:245], v217
	v_smfmac_f32_16x16x64_f16 v[230:233], v[150:153], a[160:167], v210
	v_smfmac_f32_16x16x64_f16 v[234:237], v[150:153], v[98:105], v210
	v_smfmac_f32_16x16x64_f16 v[230:233], v[154:157], a[192:199], v210
	v_smfmac_f32_16x16x64_f16 v[234:237], v[154:157], v[106:113], v210
	v_smfmac_f32_16x16x64_f16 v[230:233], v[158:161], a[224:231], v210
	v_smfmac_f32_16x16x64_f16 v[234:237], v[158:161], v[122:129], v210
	s_waitcnt lgkmcnt(1)
	v_smfmac_f32_16x16x64_f16 v[238:241], v[130:133], a[8:15], v210
	s_waitcnt lgkmcnt(0)
	v_smfmac_f32_16x16x64_f16 v[242:245], v[130:133], v[2:9], v210
	v_smfmac_f32_16x16x64_f16 v[238:241], v[134:137], a[32:39], v210
	v_fmac_f32_e32 v230, s40, v231
	v_smfmac_f32_16x16x64_f16 v[242:245], v[134:137], v[10:17], v210
	v_fmac_f32_e32 v234, s40, v235
	v_smfmac_f32_16x16x64_f16 v[238:241], v[138:141], a[72:79], v210
	v_fmac_f32_e32 v230, s41, v232
	v_smfmac_f32_16x16x64_f16 v[242:245], v[138:141], v[50:57], v210
	v_fmac_f32_e32 v234, s41, v236
	v_smfmac_f32_16x16x64_f16 v[238:241], v[142:145], a[104:111], v210
	s_nop 0
	v_permlane32_swap_b32_e32 v230, v234
	v_smfmac_f32_16x16x64_f16 v[242:245], v[142:145], v[26:33], v210
	v_add_f32_e32 v173, v230, v234
	v_smfmac_f32_16x16x64_f16 v[238:241], v[146:149], a[136:143], v210
	ds_read_b128 v[230:233], v217
	v_smfmac_f32_16x16x64_f16 v[242:245], v[146:149], v[82:89], v210
	ds_read_b128 v[234:237], v217
	v_smfmac_f32_16x16x64_f16 v[238:241], v[150:153], a[168:175], v210
	v_smfmac_f32_16x16x64_f16 v[242:245], v[150:153], v[66:73], v210
	v_smfmac_f32_16x16x64_f16 v[238:241], v[154:157], a[200:207], v210
	v_smfmac_f32_16x16x64_f16 v[242:245], v[154:157], v[114:121], v210
	v_smfmac_f32_16x16x64_f16 v[238:241], v[158:161], a[232:239], v210
	v_smfmac_f32_16x16x64_f16 v[242:245], v[158:161], v[90:97], v210
	s_nop 6
	v_fmac_f32_e32 v238, s40, v239
	v_fmac_f32_e32 v242, s40, v243
	v_fmac_f32_e32 v238, s41, v240
	v_fmac_f32_e32 v242, s41, v244
	s_nop 1
	v_permlane32_swap_b32_e32 v238, v242
	v_add_f32_e32 v172, v238, v242
	ds_read_b128 v[180:183], v199 offset:0
	ds_read_b128 v[184:187], v199 offset:1024
	ds_read_b128 v[188:191], v199 offset:4096
	ds_read_b128 v[192:195], v199 offset:5120
	ds_read_b128 v[222:225], v199 offset:8192
	ds_read_b128 v[226:229], v199 offset:9216
	v_mul_f32_e32 v239, 0x3b000000, v172
	v_mul_f32_e32 v239, v239, v196
	v_mul_f32_e32 v167, v239, v239
	v_mul_f32_e32 v239, 0x3b000000, v173
	v_mul_f32_e32 v239, v239, v179
	v_fmac_f32_e32 v167, v239, v239
	v_mul_f32_e32 v239, 0x3b000000, v175
	v_mul_f32_e32 v239, v239, v197
	v_fmac_f32_e32 v167, v239, v239
	v_mul_f32_e32 v239, 0x3b000000, v174
	v_mul_f32_e32 v239, v239, v198
	v_fmac_f32_e32 v167, v239, v239
	v_mov_b32_e32 v130, v166
	v_mov_b32_e32 v131, v167
	s_nop 0
	v_add_f32_dpp v130, v130, v130 quad_perm:[1,0,3,2] row_mask:0xf bank_mask:0xf bound_ctrl:1
	v_add_f32_dpp v131, v131, v131 quad_perm:[1,0,3,2] row_mask:0xf bank_mask:0xf bound_ctrl:1
	s_nop 0
	v_add_f32_dpp v130, v130, v130 quad_perm:[2,3,0,1] row_mask:0xf bank_mask:0xf bound_ctrl:1
	v_add_f32_dpp v131, v131, v131 quad_perm:[2,3,0,1] row_mask:0xf bank_mask:0xf bound_ctrl:1
	s_nop 0
	v_add_f32_dpp v130, v130, v130 row_half_mirror row_mask:0xf bank_mask:0xf bound_ctrl:1
	v_add_f32_dpp v131, v131, v131 row_half_mirror row_mask:0xf bank_mask:0xf bound_ctrl:1
	s_nop 0
	v_add_f32_dpp v130, v130, v130 row_mirror row_mask:0xf bank_mask:0xf bound_ctrl:1
	v_add_f32_dpp v131, v131, v131 row_mirror row_mask:0xf bank_mask:0xf bound_ctrl:1
	v_mov_b32_e32 v240, v130
	v_mov_b32_e32 v241, v131
	s_nop 0
	v_permlane32_swap_b32_e32 v130, v240
	v_permlane32_swap_b32_e32 v131, v241
	v_add_f32_e32 v130, v130, v240
	v_add_f32_e32 v131, v131, v241
	v_add_u32_e32 v242, 0, v218
	v_lshlrev_b32_e32 v243, 3, v201
	v_or_b32_e32 v243, 0x24400, v243
	s_and_saveexec_b64 s[2:3], s[4:5]
	ds_write_b64 v242, v[130:131]
	s_or_b64 exec, exec, s[2:3]
	s_waitcnt lgkmcnt(0)
	s_barrier
	ds_read_b64 v[134:135], v243 offset:0
	ds_read_b64 v[138:139], v243 offset:16
	ds_read_b64 v[142:143], v243 offset:32
	ds_read_b64 v[146:147], v243 offset:48
	s_waitcnt lgkmcnt(2)
	v_add_f32_e32 v238, v134, v138
	s_waitcnt lgkmcnt(1)
	v_add_f32_e32 v238, v238, v142
	s_waitcnt lgkmcnt(0)
	v_add_f32_e32 v238, v238, v146
	v_add_f32_e32 v239, v135, v139
	v_add_f32_e32 v239, v239, v143
	v_add_f32_e32 v239, v239, v147
	v_mul_f32_e32 v238, 0x3b000000, v238
	v_max_f32_e32 v238, 0xda24260, v238
	v_sqrt_f32_e32 v238, v238
	v_mul_f32_e32 v239, 0x3b000000, v239
	v_max_f32_e32 v239, 0xda24260, v239
	v_sqrt_f32_e32 v239, v239
	s_nop 0
	v_mov_b32_e32 v220, v239
	v_rcp_f32_e32 v240, v239
	v_min_f32_e32 v241, v238, v239
	v_mul_f32_e32 v238, 0x3c23d70a, v238
	v_mul_f32_e32 v238, v238, v240
	s_mov_b32 s52, 0x3727c5ac
	v_cmp_ngt_f32_e32 vcc, s52, v241
	v_mov_b32_e32 v240, 0x358637bd
	s_nop 1
	v_cndmask_b32_e32 v219, v240, v238, vcc
	v_mul_f32_e32 v178, 0x3b000000, v219
	v_fma_mixlo_f16 v131, v178, v173, v171
	v_fma_mixlo_f16 v139, v178, v172, v170
	v_fma_mixlo_f16 v147, v178, v175, v169
	v_fma_mixlo_f16 v155, v178, v174, v168
	v_fma_f32 v130, v178, v173, v171
	v_fma_f32 v138, v178, v172, v170
	v_fma_f32 v146, v178, v175, v169
	v_fma_f32 v154, v178, v174, v168
	v_fma_mix_f32 v130, v130, 1.0, -v131 op_sel_hi:[0,0,1]
	v_fma_mix_f32 v138, v138, 1.0, -v139 op_sel_hi:[0,0,1]
	v_fma_mix_f32 v146, v146, 1.0, -v147 op_sel_hi:[0,0,1]
	v_fma_mix_f32 v154, v154, 1.0, -v155 op_sel_hi:[0,0,1]
	v_fma_mixlo_f16 v133, v130, s42, 0
	v_fma_mixlo_f16 v141, v138, s42, 0
	v_fma_mixlo_f16 v149, v146, s42, 0
	v_fma_mixlo_f16 v157, v154, s42, 0
	v_fma_mix_f32 v130, v130, s42, -v133 op_sel_hi:[0,0,1]
	v_fma_mix_f32 v138, v138, s42, -v141 op_sel_hi:[0,0,1]
	v_fma_mix_f32 v146, v146, s42, -v149 op_sel_hi:[0,0,1]
	v_fma_mix_f32 v154, v154, s42, -v157 op_sel_hi:[0,0,1]
	v_fma_mixlo_f16 v132, v130, s42, 0
	v_fma_mixlo_f16 v140, v138, s42, 0
	v_fma_mixlo_f16 v148, v146, s42, 0
	v_fma_mixlo_f16 v156, v154, s42, 0
	ds_write_b16 v204, v131 offset:8704
	ds_write_b16 v205, v139 offset:8704
	ds_write_b16 v206, v147 offset:8704
	ds_write_b16 v207, v155 offset:8704
	ds_write_b16 v204, v133 offset:9248
	ds_write_b16 v205, v141 offset:9248
	ds_write_b16 v206, v149 offset:9248
	ds_write_b16 v207, v157 offset:9248
	ds_write_b16 v204, v132 offset:9792
	ds_write_b16 v205, v140 offset:9792
	ds_write_b16 v206, v148 offset:9792
	ds_write_b16 v207, v156 offset:9792
	s_waitcnt lgkmcnt(0)
	s_barrier
	ds_read_b128 v[130:133], v208 offset:8704
	ds_read_b128 v[134:137], v209 offset:8768
	ds_read_b128 v[138:141], v211 offset:8704
	ds_read_b128 v[142:145], v212 offset:8704
	ds_read_b128 v[146:149], v213 offset:8704
	ds_read_b128 v[150:153], v214 offset:8704
	ds_read_b128 v[154:157], v215 offset:8704
	ds_read_b128 v[158:161], v216 offset:8704
	s_waitcnt lgkmcnt(7)
	v_smfmac_f32_16x16x64_f16 v[230:233], v[130:133], a[16:23], v210
	ds_read_b128 v[238:241], v217
	v_smfmac_f32_16x16x64_f16 v[234:237], v[130:133], v[180:187], v210
	ds_read_b128 v[180:183], v199 offset:12288
	ds_read_b128 v[184:187], v199 offset:13312
	ds_read_b128 v[242:245], v217
	s_waitcnt lgkmcnt(10)
	v_smfmac_f32_16x16x64_f16 v[230:233], v[134:137], a[48:55], v210
	v_smfmac_f32_16x16x64_f16 v[234:237], v[134:137], v[188:195], v210
	ds_read_b128 v[188:191], v199 offset:16384
	ds_read_b128 v[192:195], v199 offset:17408
	s_waitcnt lgkmcnt(11)
	v_smfmac_f32_16x16x64_f16 v[230:233], v[138:141], a[80:87], v210
	v_smfmac_f32_16x16x64_f16 v[234:237], v[138:141], v[222:229], v210
	ds_read_b128 v[222:225], v199 offset:20480
	ds_read_b128 v[226:229], v199 offset:21504
	s_waitcnt lgkmcnt(12)
	v_smfmac_f32_16x16x64_f16 v[230:233], v[142:145], a[112:119], v210
	s_waitcnt lgkmcnt(5)
	v_smfmac_f32_16x16x64_f16 v[234:237], v[142:145], v[180:187], v210
	ds_read_b128 v[180:183], v199 offset:24576
	ds_read_b128 v[184:187], v199 offset:25600
	v_smfmac_f32_16x16x64_f16 v[230:233], v[146:149], a[144:151], v210
	s_waitcnt lgkmcnt(4)
	v_smfmac_f32_16x16x64_f16 v[234:237], v[146:149], v[188:195], v210
	ds_read_b128 v[188:191], v199 offset:28672
	ds_read_b128 v[192:195], v199 offset:29696
	v_smfmac_f32_16x16x64_f16 v[230:233], v[150:153], a[176:183], v210
	s_waitcnt lgkmcnt(4)
	v_smfmac_f32_16x16x64_f16 v[234:237], v[150:153], v[222:229], v210
	ds_read_b128 v[222:225], v199 offset:2048
	ds_read_b128 v[226:229], v199 offset:3072
	v_smfmac_f32_16x16x64_f16 v[230:233], v[154:157], a[208:215], v210
	s_waitcnt lgkmcnt(4)
	v_smfmac_f32_16x16x64_f16 v[234:237], v[154:157], v[180:187], v210
	ds_read_b128 v[180:183], v199 offset:6144
	ds_read_b128 v[184:187], v199 offset:7168
	v_smfmac_f32_16x16x64_f16 v[230:233], v[158:161], a[240:247], v210
	s_waitcnt lgkmcnt(4)
	v_smfmac_f32_16x16x64_f16 v[234:237], v[158:161], v[188:195], v210
	ds_read_b128 v[188:191], v199 offset:10240
	ds_read_b128 v[192:195], v199 offset:11264
	v_smfmac_f32_16x16x64_f16 v[238:241], v[130:133], a[24:31], v210
	s_waitcnt lgkmcnt(4)
	v_smfmac_f32_16x16x64_f16 v[242:245], v[130:133], v[222:229], v210
	ds_read_b128 v[222:225], v199 offset:14336
	ds_read_b128 v[226:229], v199 offset:15360
	v_smfmac_f32_16x16x64_f16 v[238:241], v[134:137], a[56:63], v210
	v_fmac_f32_e32 v230, s40, v231
	s_waitcnt lgkmcnt(4)
	v_smfmac_f32_16x16x64_f16 v[242:245], v[134:137], v[180:187], v210
	ds_read_b128 v[180:183], v199 offset:18432
	ds_read_b128 v[184:187], v199 offset:19456
	v_fmac_f32_e32 v234, s40, v235
	v_smfmac_f32_16x16x64_f16 v[238:241], v[138:141], a[88:95], v210
	v_fmac_f32_e32 v230, s41, v232
	s_waitcnt lgkmcnt(4)
	v_smfmac_f32_16x16x64_f16 v[242:245], v[138:141], v[188:195], v210
	ds_read_b128 v[188:191], v199 offset:22528
	ds_read_b128 v[192:195], v199 offset:23552
	v_fmac_f32_e32 v234, s41, v236
	v_smfmac_f32_16x16x64_f16 v[238:241], v[142:145], a[120:127], v210
	s_nop 0
	v_permlane32_swap_b32_e32 v230, v234
	s_waitcnt lgkmcnt(4)
	v_smfmac_f32_16x16x64_f16 v[242:245], v[142:145], v[222:229], v210
	ds_read_b128 v[222:225], v199 offset:26624
	ds_read_b128 v[226:229], v199 offset:27648
	v_add_f32_e32 v164, v230, v234
	v_smfmac_f32_16x16x64_f16 v[238:241], v[146:149], a[152:159], v210
	ds_read_b128 v[230:233], v217
	s_waitcnt lgkmcnt(5)
	v_smfmac_f32_16x16x64_f16 v[242:245], v[146:149], v[180:187], v210
	ds_read_b128 v[180:183], v199 offset:30720
	ds_read_b128 v[184:187], v199 offset:31744
	ds_read_b128 v[234:237], v217
	v_smfmac_f32_16x16x64_f16 v[238:241], v[150:153], a[184:191], v210
	s_waitcnt lgkmcnt(6)
	v_smfmac_f32_16x16x64_f16 v[242:245], v[150:153], v[188:195], v210
	v_smfmac_f32_16x16x64_f16 v[238:241], v[154:157], a[216:223], v210
	s_waitcnt lgkmcnt(4)
	v_smfmac_f32_16x16x64_f16 v[242:245], v[154:157], v[222:229], v210
	v_smfmac_f32_16x16x64_f16 v[238:241], v[158:161], a[248:255], v210
	s_waitcnt lgkmcnt(1)
	v_smfmac_f32_16x16x64_f16 v[242:245], v[158:161], v[180:187], v210
	v_smfmac_f32_16x16x64_f16 v[230:233], v[130:133], a[0:7], v210
	s_waitcnt lgkmcnt(0)
	v_smfmac_f32_16x16x64_f16 v[234:237], v[130:133], v[18:25], v210
	v_smfmac_f32_16x16x64_f16 v[230:233], v[134:137], a[40:47], v210
	v_fmac_f32_e32 v238, s40, v239
	v_smfmac_f32_16x16x64_f16 v[234:237], v[134:137], v[34:41], v210
	v_fmac_f32_e32 v242, s40, v243
	v_smfmac_f32_16x16x64_f16 v[230:233], v[138:141], a[64:71], v210
	v_fmac_f32_e32 v238, s41, v240
	v_smfmac_f32_16x16x64_f16 v[234:237], v[138:141], v[42:49], v210
	v_fmac_f32_e32 v242, s41, v244
	v_smfmac_f32_16x16x64_f16 v[230:233], v[142:145], a[96:103], v210
	s_nop 0
	v_permlane32_swap_b32_e32 v238, v242
	v_smfmac_f32_16x16x64_f16 v[234:237], v[142:145], v[58:65], v210
	v_add_f32_e32 v165, v238, v242
	v_smfmac_f32_16x16x64_f16 v[230:233], v[146:149], a[128:135], v210
	ds_read_b128 v[238:241], v217
	v_smfmac_f32_16x16x64_f16 v[234:237], v[146:149], v[74:81], v210
	ds_read_b128 v[242:245], v217
	v_smfmac_f32_16x16x64_f16 v[230:233], v[150:153], a[160:167], v210
	v_smfmac_f32_16x16x64_f16 v[234:237], v[150:153], v[98:105], v210
	v_smfmac_f32_16x16x64_f16 v[230:233], v[154:157], a[192:199], v210
	v_smfmac_f32_16x16x64_f16 v[234:237], v[154:157], v[106:113], v210
	v_smfmac_f32_16x16x64_f16 v[230:233], v[158:161], a[224:231], v210
	v_smfmac_f32_16x16x64_f16 v[234:237], v[158:161], v[122:129], v210
	s_waitcnt lgkmcnt(1)
	v_smfmac_f32_16x16x64_f16 v[238:241], v[130:133], a[8:15], v210
	s_waitcnt lgkmcnt(0)
	v_smfmac_f32_16x16x64_f16 v[242:245], v[130:133], v[2:9], v210
	v_smfmac_f32_16x16x64_f16 v[238:241], v[134:137], a[32:39], v210
	v_fmac_f32_e32 v230, s40, v231
	v_smfmac_f32_16x16x64_f16 v[242:245], v[134:137], v[10:17], v210
	v_fmac_f32_e32 v234, s40, v235
	v_smfmac_f32_16x16x64_f16 v[238:241], v[138:141], a[72:79], v210
	v_fmac_f32_e32 v230, s41, v232
	v_smfmac_f32_16x16x64_f16 v[242:245], v[138:141], v[50:57], v210
	v_fmac_f32_e32 v234, s41, v236
	v_smfmac_f32_16x16x64_f16 v[238:241], v[142:145], a[104:111], v210
	s_nop 0
	v_permlane32_swap_b32_e32 v230, v234
	v_smfmac_f32_16x16x64_f16 v[242:245], v[142:145], v[26:33], v210
	v_add_f32_e32 v162, v230, v234
	v_smfmac_f32_16x16x64_f16 v[238:241], v[146:149], a[136:143], v210
	ds_read_b128 v[230:233], v217
	v_smfmac_f32_16x16x64_f16 v[242:245], v[146:149], v[82:89], v210
	ds_read_b128 v[234:237], v217
	v_smfmac_f32_16x16x64_f16 v[238:241], v[150:153], a[168:175], v210
	v_smfmac_f32_16x16x64_f16 v[242:245], v[150:153], v[66:73], v210
	v_smfmac_f32_16x16x64_f16 v[238:241], v[154:157], a[200:207], v210
	v_smfmac_f32_16x16x64_f16 v[242:245], v[154:157], v[114:121], v210
	v_smfmac_f32_16x16x64_f16 v[238:241], v[158:161], a[232:239], v210
	v_smfmac_f32_16x16x64_f16 v[242:245], v[158:161], v[90:97], v210
	s_nop 6
	v_fmac_f32_e32 v238, s40, v239
	v_fmac_f32_e32 v242, s40, v243
	v_fmac_f32_e32 v238, s41, v240
	v_fmac_f32_e32 v242, s41, v244
	s_nop 1
	v_permlane32_swap_b32_e32 v238, v242
	v_add_f32_e32 v163, v238, v242
	ds_read_b128 v[180:183], v199 offset:0
	ds_read_b128 v[184:187], v199 offset:1024
	ds_read_b128 v[188:191], v199 offset:4096
	ds_read_b128 v[192:195], v199 offset:5120
	ds_read_b128 v[222:225], v199 offset:8192
	ds_read_b128 v[226:229], v199 offset:9216
	v_sub_f32_e32 v238, v163, v172
	v_mul_f32_e32 v238, 0x3b000000, v238
	v_mul_f32_e32 v238, v238, v196
	v_mul_f32_e32 v130, v238, v238
	v_sub_f32_e32 v238, v162, v173
	v_mul_f32_e32 v238, 0x3b000000, v238
	v_mul_f32_e32 v238, v238, v179
	v_fmac_f32_e32 v130, v238, v238
	v_sub_f32_e32 v238, v164, v175
	v_mul_f32_e32 v238, 0x3b000000, v238
	v_mul_f32_e32 v238, v238, v197
	v_fmac_f32_e32 v130, v238, v238
	v_sub_f32_e32 v238, v165, v174
	v_mul_f32_e32 v238, 0x3b000000, v238
	v_mul_f32_e32 v238, v238, v198
	v_fmac_f32_e32 v130, v238, v238
	s_nop 1
	v_add_f32_dpp v130, v130, v130 quad_perm:[1,0,3,2] row_mask:0xf bank_mask:0xf bound_ctrl:1
	s_nop 1
	v_add_f32_dpp v130, v130, v130 quad_perm:[2,3,0,1] row_mask:0xf bank_mask:0xf bound_ctrl:1
	s_nop 1
	v_add_f32_dpp v130, v130, v130 row_half_mirror row_mask:0xf bank_mask:0xf bound_ctrl:1
	s_nop 1
	v_add_f32_dpp v130, v130, v130 row_mirror row_mask:0xf bank_mask:0xf bound_ctrl:1
	v_mov_b32_e32 v240, v130
	s_nop 1
	v_permlane32_swap_b32_e32 v130, v240
	v_add_f32_e32 v130, v130, v240
	v_add_u32_e32 v242, 64, v218
	v_lshlrev_b32_e32 v243, 3, v201
	v_or_b32_e32 v243, 0x24440, v243
	s_and_saveexec_b64 s[2:3], s[4:5]
	ds_write_b32 v242, v130
	s_or_b64 exec, exec, s[2:3]
	s_waitcnt lgkmcnt(0)
	s_barrier
	ds_read2_b32 v[134:135], v243 offset1:4
	ds_read2_b32 v[136:137], v243 offset0:8 offset1:12
	s_waitcnt lgkmcnt(1)
	v_add_f32_e32 v238, v134, v135
	s_waitcnt lgkmcnt(0)
	v_add_f32_e32 v238, v238, v136
	v_add_f32_e32 v238, v238, v137
	v_mul_f32_e32 v238, 0x3b000000, v238
	v_max_f32_e32 v238, 0xda24260, v238
	v_rcp_f32_e32 v240, v219
	v_sqrt_f32_e32 v238, v238
	s_nop 0
	v_mul_f32_e32 v238, v240, v238
	v_max_f32_e32 v241, v220, v238
	v_mul_f32_e32 v242, 0x3a83126f, v219
	v_max_f32_e32 v242, 0x358637bd, v242
	v_max_f32_e32 v243, 0x26901d7d, v241
	v_rcp_f32_e32 v243, v243
	s_nop 0
	v_mul_f32_e32 v243, 0x3c23d70a, v243
	v_log_f32_e32 v243, v243
	s_nop 0
	v_mul_f32_e32 v243, 0x3e4ccccd, v243
	v_exp_f32_e32 v243, v243
	s_mov_b32 s52, 0x26901d7d
	v_cmp_ge_f32_e32 vcc, s52, v241
	s_nop 1
	v_cndmask_b32_e32 v243, v243, v242, vcc
	v_mul_f32_e32 v242, 0x42c80000, v219
	v_min3_f32 v1, v242, v243, 1.0
